# diff tile loop: the next tile's K/V ds_writes issued under the PV MFMAs instead of at the tile end (on top of v044)
# baseline (speedup 1.0000x reference)
.LBB0_1022:
	v_exp_f32_e32 v82, v82
	v_exp_f32_e32 v83, v83
	v_exp_f32_e32 v84, v84
	v_exp_f32_e32 v85, v85
	v_exp_f32_e32 v86, v86
	v_exp_f32_e32 v87, v87
	v_exp_f32_e32 v88, v88
	v_exp_f32_e32 v89, v89
	v_exp_f32_e32 v90, v90
	v_exp_f32_e32 v91, v91
	v_exp_f32_e32 v92, v92
	v_exp_f32_e32 v93, v93
	v_exp_f32_e32 v94, v94
	v_exp_f32_e32 v95, v95
	v_exp_f32_e32 v96, v96
	v_exp_f32_e32 v97, v97
	v_exp_f32_e32 v98, v98
	v_exp_f32_e32 v99, v99
	v_exp_f32_e32 v100, v100
	v_exp_f32_e32 v101, v101
	v_exp_f32_e32 v102, v102
	v_exp_f32_e32 v103, v103
	v_exp_f32_e32 v104, v104
	v_exp_f32_e32 v105, v105
	v_exp_f32_e32 v106, v106
	v_exp_f32_e32 v107, v107
	v_exp_f32_e32 v108, v108
	v_exp_f32_e32 v109, v109
	v_exp_f32_e32 v110, v110
	v_exp_f32_e32 v111, v111
	v_exp_f32_e32 v112, v112
	v_exp_f32_e32 v113, v113
	v_pk_add_f32 v[146:147], v[82:83], v[98:99]
	v_pk_add_f32 v[148:149], v[84:85], v[100:101]
	v_pk_add_f32 v[146:147], v[146:147], v[86:87]
	v_pk_add_f32 v[148:149], v[148:149], v[102:103]
	v_pk_add_f32 v[146:147], v[146:147], v[88:89]
	v_pk_add_f32 v[148:149], v[148:149], v[104:105]
	v_pk_add_f32 v[146:147], v[146:147], v[90:91]
	v_pk_add_f32 v[148:149], v[148:149], v[106:107]
	v_pk_add_f32 v[146:147], v[146:147], v[92:93]
	v_pk_add_f32 v[148:149], v[148:149], v[108:109]
	v_pk_add_f32 v[146:147], v[146:147], v[94:95]
	v_pk_add_f32 v[148:149], v[148:149], v[110:111]
	v_pk_add_f32 v[146:147], v[146:147], v[96:97]
	v_pk_add_f32 v[148:149], v[148:149], v[112:113]
	v_pk_add_f32 v[146:147], v[146:147], v[148:149]
	v_cvt_pk_bf16_f32 v82, v82, v83
	v_cvt_pk_bf16_f32 v83, v84, v85
	v_cvt_pk_bf16_f32 v84, v86, v87
	v_cvt_pk_bf16_f32 v85, v88, v89
	v_cvt_pk_bf16_f32 v90, v90, v91
	v_cvt_pk_bf16_f32 v91, v92, v93
	v_cvt_pk_bf16_f32 v92, v94, v95
	v_cvt_pk_bf16_f32 v93, v96, v97
	v_add_f32_e32 v146, v146, v147
	v_cvt_pk_bf16_f32 v86, v98, v99
	v_cvt_pk_bf16_f32 v87, v100, v101
	v_cvt_pk_bf16_f32 v88, v102, v103
	v_cvt_pk_bf16_f32 v89, v104, v105
	v_cvt_pk_bf16_f32 v94, v106, v107
	v_cvt_pk_bf16_f32 v95, v108, v109
	v_cvt_pk_bf16_f32 v96, v110, v111
	v_cvt_pk_bf16_f32 v97, v112, v113
	v_add3_u32 v148, s22, v240, v241
	v_add_f32_e32 v205, v205, v146
	ds_read_b64_tr_b16 v[98:99], v148 offset:17536
	ds_read_b64_tr_b16 v[100:101], v148 offset:20096
	ds_read_b64_tr_b16 v[102:103], v148 offset:22656
	ds_read_b64_tr_b16 v[104:105], v148 offset:25216
	ds_read_b64_tr_b16 v[106:107], v148 offset:27776
	ds_read_b64_tr_b16 v[108:109], v148 offset:30336
	ds_read_b64_tr_b16 v[110:111], v148 offset:32896
	ds_read_b64_tr_b16 v[112:113], v148 offset:35456
	s_waitcnt lgkmcnt(8)
	v_mfma_f32_32x32x16_bf16 v[50:65], v[150:153], v[82:85], v[50:65]
	v_mfma_f32_32x32x16_bf16 v[50:65], v[154:157], v[90:93], v[50:65]
	v_mfma_f32_32x32x16_bf16 v[50:65], v[158:161], v[86:89], v[50:65]
	v_mfma_f32_32x32x16_bf16 v[50:65], v[162:165], v[94:97], v[50:65]
	ds_read_b64_tr_b16 v[150:151], v148 offset:17600
	ds_read_b64_tr_b16 v[152:153], v148 offset:20160
	ds_read_b64_tr_b16 v[154:155], v148 offset:22720
	ds_read_b64_tr_b16 v[156:157], v148 offset:25280
	ds_read_b64_tr_b16 v[158:159], v148 offset:27840
	ds_read_b64_tr_b16 v[160:161], v148 offset:30400
	ds_read_b64_tr_b16 v[162:163], v148 offset:32960
	ds_read_b64_tr_b16 v[164:165], v148 offset:35520
	s_andn2_b64 vcc, exec, s[6:7]
	s_cbranch_vccnz .Ldiff_nowr
	s_bitcmp1_b32 s10, 0
	s_cselect_b32 s8, 0x9400, 0
	v_add_u32_e32 v146, s8, v182
	v_add_u32_e32 v147, s8, v200
	s_waitcnt vmcnt(3)
	ds_write_b128 v146, v[130:133]
	s_waitcnt vmcnt(1)
	ds_write_b128 v146, v[138:141] offset:8704
	ds_write_b128 v147, v[134:137] offset:17408
	s_waitcnt vmcnt(0)
	ds_write_b128 v147, v[142:145] offset:27648
	v_mfma_f32_32x32x16_bf16 v[34:49], v[166:169], v[82:85], v[34:49]
	v_mfma_f32_32x32x16_bf16 v[34:49], v[170:173], v[90:93], v[34:49]
	v_mfma_f32_32x32x16_bf16 v[34:49], v[174:177], v[86:89], v[34:49]
	v_mfma_f32_32x32x16_bf16 v[34:49], v[216:219], v[94:97], v[34:49]
	s_waitcnt lgkmcnt(12)
	v_mfma_f32_32x32x16_bf16 v[18:33], v[98:101], v[82:85], v[18:33]
	v_mfma_f32_32x32x16_bf16 v[18:33], v[102:105], v[90:93], v[18:33]
	v_mfma_f32_32x32x16_bf16 v[18:33], v[106:109], v[86:89], v[18:33]
	v_mfma_f32_32x32x16_bf16 v[18:33], v[110:113], v[94:97], v[18:33]
	s_waitcnt lgkmcnt(4)
	v_mfma_f32_32x32x16_bf16 v[2:17], v[150:153], v[82:85], v[2:17]
	v_mfma_f32_32x32x16_bf16 v[2:17], v[154:157], v[90:93], v[2:17]
	v_mfma_f32_32x32x16_bf16 v[2:17], v[158:161], v[86:89], v[2:17]
	v_mfma_f32_32x32x16_bf16 v[2:17], v[162:165], v[94:97], v[2:17]
	s_branch .LBB0_1007
.Ldiff_nowr:
	v_mfma_f32_32x32x16_bf16 v[34:49], v[166:169], v[82:85], v[34:49]
	v_mfma_f32_32x32x16_bf16 v[34:49], v[170:173], v[90:93], v[34:49]
	v_mfma_f32_32x32x16_bf16 v[34:49], v[174:177], v[86:89], v[34:49]
	v_mfma_f32_32x32x16_bf16 v[34:49], v[216:219], v[94:97], v[34:49]
	s_waitcnt lgkmcnt(8)
	v_mfma_f32_32x32x16_bf16 v[18:33], v[98:101], v[82:85], v[18:33]
	v_mfma_f32_32x32x16_bf16 v[18:33], v[102:105], v[90:93], v[18:33]
	v_mfma_f32_32x32x16_bf16 v[18:33], v[106:109], v[86:89], v[18:33]
	v_mfma_f32_32x32x16_bf16 v[18:33], v[110:113], v[94:97], v[18:33]
	s_waitcnt lgkmcnt(0)
	v_mfma_f32_32x32x16_bf16 v[2:17], v[150:153], v[82:85], v[2:17]
	v_mfma_f32_32x32x16_bf16 v[2:17], v[154:157], v[90:93], v[2:17]
	v_mfma_f32_32x32x16_bf16 v[2:17], v[158:161], v[86:89], v[2:17]
	v_mfma_f32_32x32x16_bf16 v[2:17], v[162:165], v[94:97], v[2:17]
	s_branch .LBB0_1007
